# P8 top-k: rank<8 test by a 32-step scalar binary search of the 8th largest key (v_cmp_ge_u32 + s_bcnt1) instead of 64 readlane/compare/add triples
# baseline (speedup 1.0000x reference)
.LBB0_760:
	v_add_u32_e32 v3, s65, v124
	v_add_u32_e32 v7, 0xfffffdfc, v3
	ds_read_b32 v4, v7
	s_waitcnt lgkmcnt(0)
	v_mul_f32_e32 v5, 0xbfb8aa3b, v4
	v_fma_f32 v8, v4, s66, -v5
	v_rndne_f32_e32 v9, v5
	v_fmac_f32_e32 v8, 0xb2a5705f, v4
	v_sub_f32_e32 v5, v5, v9
	v_add_f32_e32 v5, v5, v8
	v_cvt_i32_f32_e32 v9, v9
	v_exp_f32_e32 v5, v5
	v_cmp_nlt_f32_e32 vcc, s67, v4
	v_ldexp_f32 v5, v5, v9
	s_nop 0
	v_cndmask_b32_e32 v5, 0, v5, vcc
	v_cmp_ngt_f32_e32 vcc, s68, v4
	s_nop 1
	v_cndmask_b32_e32 v4, v194, v5, vcc
	v_add_f32_e32 v4, 1.0, v4
	v_div_scale_f32 v5, s[2:3], v4, v4, 1.0
	v_rcp_f32_e32 v8, v5
	v_div_scale_f32 v9, vcc, 1.0, v4, 1.0
	v_fma_f32 v10, -v5, v8, 1.0
	v_fmac_f32_e32 v8, v10, v8
	v_mul_f32_e32 v10, v9, v8
	v_fma_f32 v11, -v5, v10, v9
	v_fmac_f32_e32 v10, v11, v8
	v_fma_f32 v5, -v5, v10, v9
	v_div_fmas_f32 v5, v5, v8, v10
	v_div_fixup_f32 v8, v5, v4, 1.0
	s_waitcnt vmcnt(0)
	v_add_f32_e32 v9, v2, v8
	ds_write_b32 v7, v8
	s_nop 0
	v_mov_b32_dpp v4, v9 quad_perm:[1,0,3,2] row_mask:0xf bank_mask:0xf bound_ctrl:1
	v_max_f32_e32 v4, v4, v4
	v_max_f32_e32 v4, v9, v4
	s_nop 1
	v_mov_b32_dpp v5, v4 quad_perm:[2,3,0,1] row_mask:0xf bank_mask:0xf bound_ctrl:1
	v_max_f32_e32 v5, v5, v5
	v_max_f32_e32 v4, v4, v5
	s_nop 1
	v_mov_b32_dpp v5, v4 row_half_mirror row_mask:0xf bank_mask:0xf bound_ctrl:1
	v_max_f32_e32 v5, v5, v5
	v_max_f32_e32 v10, v4, v5
	v_cmp_eq_f32_e32 vcc, v9, v10
	s_nop 1
	v_lshrrev_b64 v[4:5], v120, vcc
	v_or_b32_e32 v4, 0x100, v4
	v_ffbl_b32_e32 v4, v4
	v_cmp_ne_u32_e32 vcc, v176, v4
	s_nop 1
	v_cndmask_b32_e32 v4, v195, v9, vcc
	s_nop 1
	v_mov_b32_dpp v5, v4 quad_perm:[1,0,3,2] row_mask:0xf bank_mask:0xf bound_ctrl:1
	v_max_f32_e32 v5, v5, v5
	v_max_f32_e32 v4, v4, v5
	s_nop 1
	v_mov_b32_dpp v5, v4 quad_perm:[2,3,0,1] row_mask:0xf bank_mask:0xf bound_ctrl:1
	v_max_f32_e32 v5, v5, v5
	v_max_f32_e32 v4, v4, v5
	s_nop 1
	v_mov_b32_dpp v5, v4 row_half_mirror row_mask:0xf bank_mask:0xf bound_ctrl:1
	v_max_f32_e32 v5, v5, v5
	v_max_f32_e32 v4, v4, v5
	v_add_f32_e32 v4, v10, v4
	s_nop 0
	v_readlane_b32 s2, v4, 0
	s_nop 1
	v_cmp_gt_f32_e32 vcc, s2, v4
	v_cmp_eq_f32_e64 s[2:3], s2, v4
	s_and_b64 s[2:3], s[2:3], s[6:7]
	s_or_b64 s[2:3], vcc, s[2:3]
	v_cndmask_b32_e64 v5, 0, 1, s[2:3]
	v_readlane_b32 s2, v4, 8
	s_nop 1
	v_cmp_gt_f32_e32 vcc, s2, v4
	v_cmp_eq_f32_e64 s[2:3], s2, v4
	s_and_b64 s[2:3], s[2:3], s[8:9]
	s_or_b64 s[2:3], vcc, s[2:3]
	v_cndmask_b32_e64 v10, 0, 1, s[2:3]
	v_readlane_b32 s2, v4, 16
	s_nop 1
	v_cmp_gt_f32_e32 vcc, s2, v4
	v_cmp_eq_f32_e64 s[2:3], s2, v4
	s_and_b64 s[2:3], s[2:3], s[10:11]
	s_or_b64 s[2:3], vcc, s[2:3]
	v_cndmask_b32_e64 v11, 0, 1, s[2:3]
	v_readlane_b32 s2, v4, 24
	v_add3_u32 v5, v5, v10, v11
	s_nop 0
	v_cmp_gt_f32_e32 vcc, s2, v4
	v_cmp_eq_f32_e64 s[2:3], s2, v4
	s_and_b64 s[2:3], s[2:3], s[12:13]
	s_or_b64 s[2:3], vcc, s[2:3]
	v_cndmask_b32_e64 v10, 0, 1, s[2:3]
	v_readlane_b32 s2, v4, 32
	s_nop 1
	v_cmp_gt_f32_e32 vcc, s2, v4
	v_cmp_eq_f32_e64 s[2:3], s2, v4
	s_and_b64 s[2:3], s[2:3], s[14:15]
	s_or_b64 s[2:3], vcc, s[2:3]
	v_cndmask_b32_e64 v11, 0, 1, s[2:3]
	v_readlane_b32 s2, v4, 40
	v_add3_u32 v5, v5, v10, v11
	s_nop 0
	v_cmp_gt_f32_e32 vcc, s2, v4
	v_cmp_eq_f32_e64 s[2:3], s2, v4
	s_and_b64 s[2:3], s[2:3], s[16:17]
	s_or_b64 s[2:3], vcc, s[2:3]
	v_cndmask_b32_e64 v10, 0, 1, s[2:3]
	v_readlane_b32 s2, v4, 48
	s_nop 1
	v_cmp_gt_f32_e32 vcc, s2, v4
	v_cmp_eq_f32_e64 s[2:3], s2, v4
	s_and_b64 s[2:3], s[18:19], s[2:3]
	s_or_b64 s[2:3], vcc, s[2:3]
	v_cndmask_b32_e64 v11, 0, 1, s[2:3]
	v_readlane_b32 s2, v4, 56
	s_nop 1
	v_cmp_gt_f32_e32 vcc, s2, v4
	s_nop 1
	v_addc_co_u32_e32 v4, vcc, v5, v10, vcc
	v_add_u32_e32 v4, v4, v11
	v_cmp_gt_u32_e32 vcc, 4, v4
	s_nop 1
	v_cndmask_b32_e32 v4, v195, v9, vcc
	v_ashrrev_i32_e32 v5, 31, v4
	v_and_b32_e32 v4, 0xffffffc0, v4
	v_bitop3_b32 v4, v5, v4, s69 bitop3:0x6c
	v_bitop3_b32 v4, v4, 63, v100 bitop3:0x36
	s_nop 0
	v_xor_b32_e32 v5, 0x80000000, v4
	s_mov_b32 s98, 0
	s_or_b32 s99, s98, 0x80000000
	v_cmp_ge_u32_e64 s[2:3], v5, s99
	s_bcnt1_i32_b64 s20, s[2:3]
	s_cmp_gt_u32 s20, 7
	s_cselect_b32 s98, s99, s98
	s_or_b32 s99, s98, 0x40000000
	v_cmp_ge_u32_e64 s[2:3], v5, s99
	s_bcnt1_i32_b64 s20, s[2:3]
	s_cmp_gt_u32 s20, 7
	s_cselect_b32 s98, s99, s98
	s_or_b32 s99, s98, 0x20000000
	v_cmp_ge_u32_e64 s[2:3], v5, s99
	s_bcnt1_i32_b64 s20, s[2:3]
	s_cmp_gt_u32 s20, 7
	s_cselect_b32 s98, s99, s98
	s_or_b32 s99, s98, 0x10000000
	v_cmp_ge_u32_e64 s[2:3], v5, s99
	s_bcnt1_i32_b64 s20, s[2:3]
	s_cmp_gt_u32 s20, 7
	s_cselect_b32 s98, s99, s98
	s_or_b32 s99, s98, 0x8000000
	v_cmp_ge_u32_e64 s[2:3], v5, s99
	s_bcnt1_i32_b64 s20, s[2:3]
	s_cmp_gt_u32 s20, 7
	s_cselect_b32 s98, s99, s98
	s_or_b32 s99, s98, 0x4000000
	v_cmp_ge_u32_e64 s[2:3], v5, s99
	s_bcnt1_i32_b64 s20, s[2:3]
	s_cmp_gt_u32 s20, 7
	s_cselect_b32 s98, s99, s98
	s_or_b32 s99, s98, 0x2000000
	v_cmp_ge_u32_e64 s[2:3], v5, s99
	s_bcnt1_i32_b64 s20, s[2:3]
	s_cmp_gt_u32 s20, 7
	s_cselect_b32 s98, s99, s98
	s_or_b32 s99, s98, 0x1000000
	v_cmp_ge_u32_e64 s[2:3], v5, s99
	s_bcnt1_i32_b64 s20, s[2:3]
	s_cmp_gt_u32 s20, 7
	s_cselect_b32 s98, s99, s98
	s_or_b32 s99, s98, 0x800000
	v_cmp_ge_u32_e64 s[2:3], v5, s99
	s_bcnt1_i32_b64 s20, s[2:3]
	s_cmp_gt_u32 s20, 7
	s_cselect_b32 s98, s99, s98
	s_or_b32 s99, s98, 0x400000
	v_cmp_ge_u32_e64 s[2:3], v5, s99
	s_bcnt1_i32_b64 s20, s[2:3]
	s_cmp_gt_u32 s20, 7
	s_cselect_b32 s98, s99, s98
	s_or_b32 s99, s98, 0x200000
	v_cmp_ge_u32_e64 s[2:3], v5, s99
	s_bcnt1_i32_b64 s20, s[2:3]
	s_cmp_gt_u32 s20, 7
	s_cselect_b32 s98, s99, s98
	s_or_b32 s99, s98, 0x100000
	v_cmp_ge_u32_e64 s[2:3], v5, s99
	s_bcnt1_i32_b64 s20, s[2:3]
	s_cmp_gt_u32 s20, 7
	s_cselect_b32 s98, s99, s98
	s_or_b32 s99, s98, 0x80000
	v_cmp_ge_u32_e64 s[2:3], v5, s99
	s_bcnt1_i32_b64 s20, s[2:3]
	s_cmp_gt_u32 s20, 7
	s_cselect_b32 s98, s99, s98
	s_or_b32 s99, s98, 0x40000
	v_cmp_ge_u32_e64 s[2:3], v5, s99
	s_bcnt1_i32_b64 s20, s[2:3]
	s_cmp_gt_u32 s20, 7
	s_cselect_b32 s98, s99, s98
	s_or_b32 s99, s98, 0x20000
	v_cmp_ge_u32_e64 s[2:3], v5, s99
	s_bcnt1_i32_b64 s20, s[2:3]
	s_cmp_gt_u32 s20, 7
	s_cselect_b32 s98, s99, s98
	s_or_b32 s99, s98, 0x10000
	v_cmp_ge_u32_e64 s[2:3], v5, s99
	s_bcnt1_i32_b64 s20, s[2:3]
	s_cmp_gt_u32 s20, 7
	s_cselect_b32 s98, s99, s98
	s_or_b32 s99, s98, 0x8000
	v_cmp_ge_u32_e64 s[2:3], v5, s99
	s_bcnt1_i32_b64 s20, s[2:3]
	s_cmp_gt_u32 s20, 7
	s_cselect_b32 s98, s99, s98
	s_or_b32 s99, s98, 0x4000
	v_cmp_ge_u32_e64 s[2:3], v5, s99
	s_bcnt1_i32_b64 s20, s[2:3]
	s_cmp_gt_u32 s20, 7
	s_cselect_b32 s98, s99, s98
	s_or_b32 s99, s98, 0x2000
	v_cmp_ge_u32_e64 s[2:3], v5, s99
	s_bcnt1_i32_b64 s20, s[2:3]
	s_cmp_gt_u32 s20, 7
	s_cselect_b32 s98, s99, s98
	s_or_b32 s99, s98, 0x1000
	v_cmp_ge_u32_e64 s[2:3], v5, s99
	s_bcnt1_i32_b64 s20, s[2:3]
	s_cmp_gt_u32 s20, 7
	s_cselect_b32 s98, s99, s98
	s_or_b32 s99, s98, 0x800
	v_cmp_ge_u32_e64 s[2:3], v5, s99
	s_bcnt1_i32_b64 s20, s[2:3]
	s_cmp_gt_u32 s20, 7
	s_cselect_b32 s98, s99, s98
	s_or_b32 s99, s98, 0x400
	v_cmp_ge_u32_e64 s[2:3], v5, s99
	s_bcnt1_i32_b64 s20, s[2:3]
	s_cmp_gt_u32 s20, 7
	s_cselect_b32 s98, s99, s98
	s_or_b32 s99, s98, 0x200
	v_cmp_ge_u32_e64 s[2:3], v5, s99
	s_bcnt1_i32_b64 s20, s[2:3]
	s_cmp_gt_u32 s20, 7
	s_cselect_b32 s98, s99, s98
	s_or_b32 s99, s98, 0x100
	v_cmp_ge_u32_e64 s[2:3], v5, s99
	s_bcnt1_i32_b64 s20, s[2:3]
	s_cmp_gt_u32 s20, 7
	s_cselect_b32 s98, s99, s98
	s_or_b32 s99, s98, 0x80
	v_cmp_ge_u32_e64 s[2:3], v5, s99
	s_bcnt1_i32_b64 s20, s[2:3]
	s_cmp_gt_u32 s20, 7
	s_cselect_b32 s98, s99, s98
	s_or_b32 s99, s98, 0x40
	v_cmp_ge_u32_e64 s[2:3], v5, s99
	s_bcnt1_i32_b64 s20, s[2:3]
	s_cmp_gt_u32 s20, 7
	s_cselect_b32 s98, s99, s98
	s_or_b32 s99, s98, 0x20
	v_cmp_ge_u32_e64 s[2:3], v5, s99
	s_bcnt1_i32_b64 s20, s[2:3]
	s_cmp_gt_u32 s20, 7
	s_cselect_b32 s98, s99, s98
	s_or_b32 s99, s98, 0x10
	v_cmp_ge_u32_e64 s[2:3], v5, s99
	s_bcnt1_i32_b64 s20, s[2:3]
	s_cmp_gt_u32 s20, 7
	s_cselect_b32 s98, s99, s98
	s_or_b32 s99, s98, 0x8
	v_cmp_ge_u32_e64 s[2:3], v5, s99
	s_bcnt1_i32_b64 s20, s[2:3]
	s_cmp_gt_u32 s20, 7
	s_cselect_b32 s98, s99, s98
	s_or_b32 s99, s98, 0x4
	v_cmp_ge_u32_e64 s[2:3], v5, s99
	s_bcnt1_i32_b64 s20, s[2:3]
	s_cmp_gt_u32 s20, 7
	s_cselect_b32 s98, s99, s98
	s_or_b32 s99, s98, 0x2
	v_cmp_ge_u32_e64 s[2:3], v5, s99
	s_bcnt1_i32_b64 s20, s[2:3]
	s_cmp_gt_u32 s20, 7
	s_cselect_b32 s98, s99, s98
	s_or_b32 s99, s98, 0x1
	v_cmp_ge_u32_e64 s[2:3], v5, s99
	s_bcnt1_i32_b64 s20, s[2:3]
	s_cmp_gt_u32 s20, 7
	s_cselect_b32 s98, s99, s98
	v_cmp_ge_u32_e64 s[2:3], v5, s98
	s_and_b64 s[20:21], vcc, s[2:3]
	v_cndmask_b32_e64 v4, 0, v8, s[20:21]
	s_nop 1
	v_add_f32_dpp v4, v4, v4 quad_perm:[1,0,3,2] row_mask:0xf bank_mask:0xf bound_ctrl:1
	s_nop 1
	v_add_f32_dpp v4, v4, v4 quad_perm:[2,3,0,1] row_mask:0xf bank_mask:0xf bound_ctrl:1
	s_nop 1
	v_add_f32_dpp v4, v4, v4 row_half_mirror row_mask:0xf bank_mask:0xf bound_ctrl:1
	s_nop 1
	v_add_f32_dpp v4, v4, v4 row_mirror row_mask:0xf bank_mask:0xf bound_ctrl:1
	s_nop 0
	v_readlane_b32 s22, v4, 0
	v_readlane_b32 s38, v4, 16
	v_readlane_b32 s23, v4, 32
	v_readlane_b32 s39, v4, 48
	s_and_saveexec_b64 s[2:3], s[4:5]
	s_cbranch_execz .LBB0_762
	v_mov_b32_e32 v4, s38
	v_mov_b32_e32 v5, s39
	v_pk_add_f32 v[4:5], s[22:23], v[4:5]
	s_nop 0
	v_add_f32_e32 v4, v4, v5
	v_add_f32_e32 v4, 0x1e3ce508, v4
	v_div_scale_f32 v5, s[22:23], v4, v4, s70
	v_rcp_f32_e32 v7, v5
	s_add_i32 s22, s65, 0xfffffefc
	v_fma_f32 v8, -v5, v7, 1.0
	v_fmac_f32_e32 v7, v8, v7
	v_div_scale_f32 v8, vcc, s70, v4, s70
	v_mul_f32_e32 v9, v8, v7
	v_fma_f32 v10, -v5, v9, v8
	v_fmac_f32_e32 v9, v10, v7
	v_fma_f32 v5, -v5, v9, v8
	v_div_fmas_f32 v5, v5, v7, v9
	v_div_fixup_f32 v4, v5, v4, s70
	v_mov_b32_e32 v5, s22
	ds_write_b32 v5, v4
.LBB0_762:
	s_or_b64 exec, exec, s[2:3]
	v_add_u32_e32 v3, 0xffffff00, v3
	ds_read_b32 v4, v3
	s_waitcnt lgkmcnt(0)
	v_mul_f32_e32 v5, 0xbfb8aa3b, v4
	v_fma_f32 v7, v4, s66, -v5
	v_rndne_f32_e32 v8, v5
	v_fmac_f32_e32 v7, 0xb2a5705f, v4
	v_sub_f32_e32 v5, v5, v8
	v_add_f32_e32 v5, v5, v7
	v_cvt_i32_f32_e32 v8, v8
	v_exp_f32_e32 v5, v5
	v_cmp_nlt_f32_e32 vcc, s67, v4
	v_ldexp_f32 v5, v5, v8
	s_nop 0
	v_cndmask_b32_e32 v5, 0, v5, vcc
	v_cmp_ngt_f32_e32 vcc, s68, v4
	s_nop 1
	v_cndmask_b32_e32 v4, v194, v5, vcc
	v_add_f32_e32 v4, 1.0, v4
	v_div_scale_f32 v5, s[2:3], v4, v4, 1.0
	v_rcp_f32_e32 v7, v5
	v_div_scale_f32 v8, vcc, 1.0, v4, 1.0
	v_fma_f32 v9, -v5, v7, 1.0
	v_fmac_f32_e32 v7, v9, v7
	v_mul_f32_e32 v9, v8, v7
	v_fma_f32 v10, -v5, v9, v8
	v_fmac_f32_e32 v9, v10, v7
	v_fma_f32 v5, -v5, v9, v8
	v_div_fmas_f32 v5, v5, v7, v9
	v_div_fixup_f32 v7, v5, v4, 1.0
	v_add_f32_e32 v8, v2, v7
	ds_write_b32 v3, v7
	s_nop 0
	v_mov_b32_dpp v4, v8 quad_perm:[1,0,3,2] row_mask:0xf bank_mask:0xf bound_ctrl:1
	v_max_f32_e32 v4, v4, v4
	v_max_f32_e32 v4, v8, v4
	s_nop 1
	v_mov_b32_dpp v5, v4 quad_perm:[2,3,0,1] row_mask:0xf bank_mask:0xf bound_ctrl:1
	v_max_f32_e32 v5, v5, v5
	v_max_f32_e32 v4, v4, v5
	s_nop 1
	v_mov_b32_dpp v5, v4 row_half_mirror row_mask:0xf bank_mask:0xf bound_ctrl:1
	v_max_f32_e32 v5, v5, v5
	v_max_f32_e32 v9, v4, v5
	v_cmp_eq_f32_e32 vcc, v8, v9
	s_nop 1
	v_lshrrev_b64 v[4:5], v120, vcc
	v_or_b32_e32 v4, 0x100, v4
	v_ffbl_b32_e32 v4, v4
	v_cmp_ne_u32_e32 vcc, v176, v4
	s_nop 1
	v_cndmask_b32_e32 v4, v195, v8, vcc
	s_nop 1
	v_mov_b32_dpp v5, v4 quad_perm:[1,0,3,2] row_mask:0xf bank_mask:0xf bound_ctrl:1
	v_max_f32_e32 v5, v5, v5
	v_max_f32_e32 v4, v4, v5
	s_nop 1
	v_mov_b32_dpp v5, v4 quad_perm:[2,3,0,1] row_mask:0xf bank_mask:0xf bound_ctrl:1
	v_max_f32_e32 v5, v5, v5
	v_max_f32_e32 v4, v4, v5
	s_nop 1
	v_mov_b32_dpp v5, v4 row_half_mirror row_mask:0xf bank_mask:0xf bound_ctrl:1
	v_max_f32_e32 v5, v5, v5
	v_max_f32_e32 v4, v4, v5
	v_add_f32_e32 v4, v9, v4
	s_nop 0
	v_readlane_b32 s2, v4, 0
	s_nop 1
	v_cmp_gt_f32_e32 vcc, s2, v4
	v_cmp_eq_f32_e64 s[2:3], s2, v4
	s_and_b64 s[2:3], s[2:3], s[6:7]
	s_or_b64 s[2:3], vcc, s[2:3]
	v_cndmask_b32_e64 v5, 0, 1, s[2:3]
	v_readlane_b32 s2, v4, 8
	s_nop 1
	v_cmp_gt_f32_e32 vcc, s2, v4
	v_cmp_eq_f32_e64 s[2:3], s2, v4
	s_and_b64 s[2:3], s[2:3], s[8:9]
	s_or_b64 s[2:3], vcc, s[2:3]
	v_cndmask_b32_e64 v9, 0, 1, s[2:3]
	v_readlane_b32 s2, v4, 16
	s_nop 1
	v_cmp_gt_f32_e32 vcc, s2, v4
	v_cmp_eq_f32_e64 s[2:3], s2, v4
	s_and_b64 s[2:3], s[2:3], s[10:11]
	s_or_b64 s[2:3], vcc, s[2:3]
	v_cndmask_b32_e64 v10, 0, 1, s[2:3]
	v_readlane_b32 s2, v4, 24
	v_add3_u32 v5, v5, v9, v10
	s_nop 0
	v_cmp_gt_f32_e32 vcc, s2, v4
	v_cmp_eq_f32_e64 s[2:3], s2, v4
	s_and_b64 s[2:3], s[2:3], s[12:13]
	s_or_b64 s[2:3], vcc, s[2:3]
	v_cndmask_b32_e64 v9, 0, 1, s[2:3]
	v_readlane_b32 s2, v4, 32
	s_nop 1
	v_cmp_gt_f32_e32 vcc, s2, v4
	v_cmp_eq_f32_e64 s[2:3], s2, v4
	s_and_b64 s[2:3], s[2:3], s[14:15]
	s_or_b64 s[2:3], vcc, s[2:3]
	v_cndmask_b32_e64 v10, 0, 1, s[2:3]
	v_readlane_b32 s2, v4, 40
	v_add3_u32 v5, v5, v9, v10
	s_nop 0
	v_cmp_gt_f32_e32 vcc, s2, v4
	v_cmp_eq_f32_e64 s[2:3], s2, v4
	s_and_b64 s[2:3], s[2:3], s[16:17]
	s_or_b64 s[2:3], vcc, s[2:3]
	v_cndmask_b32_e64 v9, 0, 1, s[2:3]
	v_readlane_b32 s2, v4, 48
	s_nop 1
	v_cmp_gt_f32_e32 vcc, s2, v4
	v_cmp_eq_f32_e64 s[2:3], s2, v4
	s_and_b64 s[2:3], s[18:19], s[2:3]
	s_or_b64 s[2:3], vcc, s[2:3]
	v_cndmask_b32_e64 v10, 0, 1, s[2:3]
	v_readlane_b32 s2, v4, 56
	s_nop 1
	v_cmp_gt_f32_e32 vcc, s2, v4
	s_nop 1
	v_addc_co_u32_e32 v4, vcc, v5, v9, vcc
	v_add_u32_e32 v4, v4, v10
	v_cmp_gt_u32_e32 vcc, 4, v4
	s_nop 1
	v_cndmask_b32_e32 v4, v195, v8, vcc
	v_ashrrev_i32_e32 v5, 31, v4
	v_and_b32_e32 v4, 0xffffffc0, v4
	v_bitop3_b32 v4, v5, v4, s69 bitop3:0x6c
	v_bitop3_b32 v4, v4, 63, v100 bitop3:0x36
	s_nop 0
	v_xor_b32_e32 v5, 0x80000000, v4
	s_mov_b32 s98, 0
	s_or_b32 s99, s98, 0x80000000
	v_cmp_ge_u32_e64 s[2:3], v5, s99
	s_bcnt1_i32_b64 s22, s[2:3]
	s_cmp_gt_u32 s22, 7
	s_cselect_b32 s98, s99, s98
	s_or_b32 s99, s98, 0x40000000
	v_cmp_ge_u32_e64 s[2:3], v5, s99
	s_bcnt1_i32_b64 s22, s[2:3]
	s_cmp_gt_u32 s22, 7
	s_cselect_b32 s98, s99, s98
	s_or_b32 s99, s98, 0x20000000
	v_cmp_ge_u32_e64 s[2:3], v5, s99
	s_bcnt1_i32_b64 s22, s[2:3]
	s_cmp_gt_u32 s22, 7
	s_cselect_b32 s98, s99, s98
	s_or_b32 s99, s98, 0x10000000
	v_cmp_ge_u32_e64 s[2:3], v5, s99
	s_bcnt1_i32_b64 s22, s[2:3]
	s_cmp_gt_u32 s22, 7
	s_cselect_b32 s98, s99, s98
	s_or_b32 s99, s98, 0x8000000
	v_cmp_ge_u32_e64 s[2:3], v5, s99
	s_bcnt1_i32_b64 s22, s[2:3]
	s_cmp_gt_u32 s22, 7
	s_cselect_b32 s98, s99, s98
	s_or_b32 s99, s98, 0x4000000
	v_cmp_ge_u32_e64 s[2:3], v5, s99
	s_bcnt1_i32_b64 s22, s[2:3]
	s_cmp_gt_u32 s22, 7
	s_cselect_b32 s98, s99, s98
	s_or_b32 s99, s98, 0x2000000
	v_cmp_ge_u32_e64 s[2:3], v5, s99
	s_bcnt1_i32_b64 s22, s[2:3]
	s_cmp_gt_u32 s22, 7
	s_cselect_b32 s98, s99, s98
	s_or_b32 s99, s98, 0x1000000
	v_cmp_ge_u32_e64 s[2:3], v5, s99
	s_bcnt1_i32_b64 s22, s[2:3]
	s_cmp_gt_u32 s22, 7
	s_cselect_b32 s98, s99, s98
	s_or_b32 s99, s98, 0x800000
	v_cmp_ge_u32_e64 s[2:3], v5, s99
	s_bcnt1_i32_b64 s22, s[2:3]
	s_cmp_gt_u32 s22, 7
	s_cselect_b32 s98, s99, s98
	s_or_b32 s99, s98, 0x400000
	v_cmp_ge_u32_e64 s[2:3], v5, s99
	s_bcnt1_i32_b64 s22, s[2:3]
	s_cmp_gt_u32 s22, 7
	s_cselect_b32 s98, s99, s98
	s_or_b32 s99, s98, 0x200000
	v_cmp_ge_u32_e64 s[2:3], v5, s99
	s_bcnt1_i32_b64 s22, s[2:3]
	s_cmp_gt_u32 s22, 7
	s_cselect_b32 s98, s99, s98
	s_or_b32 s99, s98, 0x100000
	v_cmp_ge_u32_e64 s[2:3], v5, s99
	s_bcnt1_i32_b64 s22, s[2:3]
	s_cmp_gt_u32 s22, 7
	s_cselect_b32 s98, s99, s98
	s_or_b32 s99, s98, 0x80000
	v_cmp_ge_u32_e64 s[2:3], v5, s99
	s_bcnt1_i32_b64 s22, s[2:3]
	s_cmp_gt_u32 s22, 7
	s_cselect_b32 s98, s99, s98
	s_or_b32 s99, s98, 0x40000
	v_cmp_ge_u32_e64 s[2:3], v5, s99
	s_bcnt1_i32_b64 s22, s[2:3]
	s_cmp_gt_u32 s22, 7
	s_cselect_b32 s98, s99, s98
	s_or_b32 s99, s98, 0x20000
	v_cmp_ge_u32_e64 s[2:3], v5, s99
	s_bcnt1_i32_b64 s22, s[2:3]
	s_cmp_gt_u32 s22, 7
	s_cselect_b32 s98, s99, s98
	s_or_b32 s99, s98, 0x10000
	v_cmp_ge_u32_e64 s[2:3], v5, s99
	s_bcnt1_i32_b64 s22, s[2:3]
	s_cmp_gt_u32 s22, 7
	s_cselect_b32 s98, s99, s98
	s_or_b32 s99, s98, 0x8000
	v_cmp_ge_u32_e64 s[2:3], v5, s99
	s_bcnt1_i32_b64 s22, s[2:3]
	s_cmp_gt_u32 s22, 7
	s_cselect_b32 s98, s99, s98
	s_or_b32 s99, s98, 0x4000
	v_cmp_ge_u32_e64 s[2:3], v5, s99
	s_bcnt1_i32_b64 s22, s[2:3]
	s_cmp_gt_u32 s22, 7
	s_cselect_b32 s98, s99, s98
	s_or_b32 s99, s98, 0x2000
	v_cmp_ge_u32_e64 s[2:3], v5, s99
	s_bcnt1_i32_b64 s22, s[2:3]
	s_cmp_gt_u32 s22, 7
	s_cselect_b32 s98, s99, s98
	s_or_b32 s99, s98, 0x1000
	v_cmp_ge_u32_e64 s[2:3], v5, s99
	s_bcnt1_i32_b64 s22, s[2:3]
	s_cmp_gt_u32 s22, 7
	s_cselect_b32 s98, s99, s98
	s_or_b32 s99, s98, 0x800
	v_cmp_ge_u32_e64 s[2:3], v5, s99
	s_bcnt1_i32_b64 s22, s[2:3]
	s_cmp_gt_u32 s22, 7
	s_cselect_b32 s98, s99, s98
	s_or_b32 s99, s98, 0x400
	v_cmp_ge_u32_e64 s[2:3], v5, s99
	s_bcnt1_i32_b64 s22, s[2:3]
	s_cmp_gt_u32 s22, 7
	s_cselect_b32 s98, s99, s98
	s_or_b32 s99, s98, 0x200
	v_cmp_ge_u32_e64 s[2:3], v5, s99
	s_bcnt1_i32_b64 s22, s[2:3]
	s_cmp_gt_u32 s22, 7
	s_cselect_b32 s98, s99, s98
	s_or_b32 s99, s98, 0x100
	v_cmp_ge_u32_e64 s[2:3], v5, s99
	s_bcnt1_i32_b64 s22, s[2:3]
	s_cmp_gt_u32 s22, 7
	s_cselect_b32 s98, s99, s98
	s_or_b32 s99, s98, 0x80
	v_cmp_ge_u32_e64 s[2:3], v5, s99
	s_bcnt1_i32_b64 s22, s[2:3]
	s_cmp_gt_u32 s22, 7
	s_cselect_b32 s98, s99, s98
	s_or_b32 s99, s98, 0x40
	v_cmp_ge_u32_e64 s[2:3], v5, s99
	s_bcnt1_i32_b64 s22, s[2:3]
	s_cmp_gt_u32 s22, 7
	s_cselect_b32 s98, s99, s98
	s_or_b32 s99, s98, 0x20
	v_cmp_ge_u32_e64 s[2:3], v5, s99
	s_bcnt1_i32_b64 s22, s[2:3]
	s_cmp_gt_u32 s22, 7
	s_cselect_b32 s98, s99, s98
	s_or_b32 s99, s98, 0x10
	v_cmp_ge_u32_e64 s[2:3], v5, s99
	s_bcnt1_i32_b64 s22, s[2:3]
	s_cmp_gt_u32 s22, 7
	s_cselect_b32 s98, s99, s98
	s_or_b32 s99, s98, 0x8
	v_cmp_ge_u32_e64 s[2:3], v5, s99
	s_bcnt1_i32_b64 s22, s[2:3]
	s_cmp_gt_u32 s22, 7
	s_cselect_b32 s98, s99, s98
	s_or_b32 s99, s98, 0x4
	v_cmp_ge_u32_e64 s[2:3], v5, s99
	s_bcnt1_i32_b64 s22, s[2:3]
	s_cmp_gt_u32 s22, 7
	s_cselect_b32 s98, s99, s98
	s_or_b32 s99, s98, 0x2
	v_cmp_ge_u32_e64 s[2:3], v5, s99
	s_bcnt1_i32_b64 s22, s[2:3]
	s_cmp_gt_u32 s22, 7
	s_cselect_b32 s98, s99, s98
	s_or_b32 s99, s98, 0x1
	v_cmp_ge_u32_e64 s[2:3], v5, s99
	s_bcnt1_i32_b64 s22, s[2:3]
	s_cmp_gt_u32 s22, 7
	s_cselect_b32 s98, s99, s98
	v_cmp_ge_u32_e64 s[2:3], v5, s98
	s_and_b64 s[22:23], vcc, s[2:3]
	v_cndmask_b32_e64 v4, 0, v7, s[22:23]
	s_nop 1
	v_add_f32_dpp v4, v4, v4 quad_perm:[1,0,3,2] row_mask:0xf bank_mask:0xf bound_ctrl:1
	s_nop 1
	v_add_f32_dpp v4, v4, v4 quad_perm:[2,3,0,1] row_mask:0xf bank_mask:0xf bound_ctrl:1
	s_nop 1
	v_add_f32_dpp v4, v4, v4 row_half_mirror row_mask:0xf bank_mask:0xf bound_ctrl:1
	s_nop 1
	v_add_f32_dpp v4, v4, v4 row_mirror row_mask:0xf bank_mask:0xf bound_ctrl:1
	s_nop 0
	v_readlane_b32 s38, v4, 0
	v_readlane_b32 s72, v4, 16
	v_readlane_b32 s39, v4, 32
	v_readlane_b32 s73, v4, 48
	s_and_saveexec_b64 s[2:3], s[4:5]
	s_cbranch_execz .LBB0_759
	v_mov_b32_e32 v4, s72
	v_mov_b32_e32 v5, s73
	v_pk_add_f32 v[4:5], s[38:39], v[4:5]
	s_nop 0
	v_add_f32_e32 v3, v4, v5
	v_add_f32_e32 v3, 0x1e3ce508, v3
	v_div_scale_f32 v4, s[38:39], v3, v3, s70
	v_rcp_f32_e32 v5, v4
	s_nop 0
	v_fma_f32 v7, -v4, v5, 1.0
	v_fmac_f32_e32 v5, v7, v5
	v_div_scale_f32 v7, vcc, s70, v3, s70
	v_mul_f32_e32 v8, v7, v5
	v_fma_f32 v9, -v4, v8, v7
	v_fmac_f32_e32 v8, v9, v5
	v_fma_f32 v4, -v4, v8, v7
	v_div_fmas_f32 v4, v4, v5, v8
	v_div_fixup_f32 v3, v4, v3, s70
	v_mov_b32_e32 v4, s65
	ds_write_b32 v4, v3
	s_branch .LBB0_759
